# ph3 pre-norm row loads non-temporal as well
# baseline (speedup 1.0000x reference)
; #define LAS __attribute__((address_space(3)))
; __device__ __forceinline__ void unpack8(const u32x4 w, float (&f)[8]) { f[0] = bf_lo(w.x); f[1] = bf_hi(w.x); f[2] = bf_lo(w.y); f[3] = bf_hi(w.y); f[4] = bf_lo(w.z); f[5] = bf_hi(w.z); f[6] = bf_lo(w.w); f[7] = bf_hi(w.w); }
; __device__ __forceinline__ u32x4 pack8(const float (&f)[8]) { u32x4 o; o.x = cvt_pk_bf16(f[0], f[1]); o.y = cvt_pk_bf16(f[2], f[3]); o.z = cvt_pk_bf16(f[4], f[5]); o.w = cvt_pk_bf16(f[6], f[7]); return o; }
; #define PHASE_IDS() int lane = lane_id(); asm volatile("" : "+v"(lane)); const int wave = wave_s, tid = wave_s * 64 + lane, gw = vcu * NWAVES + wave; (void)tid; (void)gw
; __global__ void __launch_bounds__(NWAVES * 64, 2) mk_fwd(Args args) {
;     ...
;             PHASE_IDS();
;             constexpr int XS = 1028;
;             LAS float* XL = (LAS float*)lds;
;             LAS float* PART = (LAS float*)(lds + 65792);
;             LAS float* LOG = (LAS float*)(lds + 82176);
;             LAS int* LCNT = (LAS int*)(lds + 84224);
;             LAS int* GBASE = (LAS int*)(lds + 84352);
;             LAS i32x4* REC = (LAS i32x4*)(lds + 84480);
;             LAS float* TSC = (LAS float*)(lds + 122880);
;             LAS float* TOP = (LAS float*)(lds + 124928);
;             const float* lng = args.in[15] + (size_t)(layer * 2 + 0) * D; const float* lnb = args.in[16] + (size_t)(layer * 2 + 0) * D;
;             const float* rw = args.in[9] + (size_t)layer * D * NEXP; const float* rb = args.in[10] + layer * NEXP;
;             if (tid < 32) LCNT[tid] = 0;
;             __syncthreads();
;             const int tk = lane & 15, kq = lane >> 4;
;             auto split8 = [](const float (&f)[8], bf16x8& hi, bf16x8& lo) { const u32x4 h = pack8(f); float fh[8], fl[8]; unpack8(h, fh);
; #pragma unroll
;                 for (int i = 0; i < 8; ++i) fl[i] = f[i] - fh[i];
;                 hi = __builtin_bit_cast(bf16x8, h); lo = __builtin_bit_cast(bf16x8, pack8(fl)); };
;             bf16x8 rwh[4][2], rwl[4][2];
; #pragma unroll
;             for (int ks = 0; ks < 4; ++ks)
; #pragma unroll
;                 for (int tile = 0; tile < 2; ++tile) { float f[8];
; #pragma unroll
;                     for (int j = 0; j < 8; ++j) f[j] = rw[(size_t)(128 * wave + 32 * ks + 8 * kq + j) * NEXP + 16 * tile + tk];
;                     split8(f, rwh[ks][tile], rwl[ks][tile]); }
.LBB0_481:
	s_mov_b32 s2, -1
	s_waitcnt lgkmcnt(0)
	s_barrier
	s_nop 0
	v_mbcnt_lo_u32_b32 v0, s2, 0
	v_mbcnt_hi_u32_b32 v106, s2, v0
	v_readlane_b32 s2, v253, 9
	s_nop 1
	v_add_u32_e32 v94, s2, v106
	v_cmp_gt_i32_e64 s[2:3], 32, v94
	v_lshl_add_u32 v107, v94, 2, 0
	s_and_saveexec_b64 s[4:5], s[2:3]
	v_add_u32_e32 v0, 0x14900, v107
	ds_write_b32 v0, v33
	s_or_b64 exec, exec, s[4:5]
	v_readlane_b32 s8, v252, 43
	s_lshl_b32 s4, s66, 11
	v_readlane_b32 s16, v252, 51
	v_readlane_b32 s17, v252, 52
	v_readlane_b32 s18, v252, 53
	v_readlane_b32 s19, v252, 54
	v_readlane_b32 s20, v252, 55
	v_readlane_b32 s21, v252, 56
	s_mov_b32 s5, s69
	s_mov_b32 s6, s4
	v_readlane_b32 s22, v252, 57
	v_readlane_b32 s23, v252, 58
	s_mov_b64 s[16:17], s[20:21]
	v_writelane_b32 v254, s6, 40
	s_lshl_b64 s[4:5], s[4:5], 2
	s_mov_b64 s[18:19], s[22:23]
	v_writelane_b32 v254, s7, 41
	v_readlane_b32 s9, v252, 44
	v_readlane_b32 s10, v252, 45
	v_readlane_b32 s11, v252, 46
	s_add_u32 s6, s18, s4
	s_addc_u32 s7, s19, s5
	v_readlane_b32 s8, v252, 0
	v_writelane_b32 v254, s6, 48
	v_readlane_b32 s9, v252, 1
	s_add_u32 s4, s8, s4
	v_writelane_b32 v254, s7, 49
	s_addc_u32 s5, s9, s5
	v_writelane_b32 v254, s4, 44
	s_mov_b32 s67, s69
	s_lshl_b64 s[40:41], s[66:67], 17
	v_writelane_b32 v254, s5, 45
	v_readlane_b32 s4, v253, 25
	v_readlane_b32 s5, v253, 26
	s_andn2_b64 vcc, exec, s[4:5]
	s_mov_b32 s6, 0
	v_readlane_b32 s12, v252, 47
	v_readlane_b32 s13, v252, 48
	v_readlane_b32 s14, v252, 49
	v_readlane_b32 s15, v252, 50
	v_readlane_b32 s10, v252, 2
	v_readlane_b32 s11, v252, 3
	s_waitcnt lgkmcnt(0)
	s_barrier
	s_cbranch_vccnz .LBB0_496
	s_lshl_b32 s68, s66, 5
	v_readlane_b32 s8, v252, 43
	s_lshl_b64 s[4:5], s[68:69], 2
	v_readlane_b32 s12, v252, 47
	v_readlane_b32 s13, v252, 48
	s_add_u32 s6, s12, s4
	v_lshlrev_b32_e32 v2, 3, v106
	s_addc_u32 s7, s13, s5
	v_ashrrev_i32_e32 v3, 31, v2
	v_readlane_b32 s4, v254, 48
	v_lshlrev_b64 v[0:1], 2, v[2:3]
	v_readlane_b32 s5, v254, 49
	v_readlane_b32 s9, v252, 44
	v_ashrrev_i32_e32 v5, 4, v106
	v_lshl_add_u64 v[96:97], s[4:5], 0, v[0:1]
	v_readlane_b32 s4, v254, 44
	v_readlane_b32 s5, v254, 45
	v_lshlrev_b32_e32 v6, 2, v94
	v_readlane_b32 s13, v255, 41
	v_lshl_add_u64 v[98:99], s[4:5], 0, v[0:1]
	v_and_b32_e32 v0, 31, v106
	v_lshlrev_b32_e32 v32, 2, v0
	v_readlane_b32 s8, v253, 28
	v_readlane_b32 s10, v252, 45
	v_and_b32_e32 v4, 15, v106
	v_ashrrev_i32_e32 v95, 5, v94
	v_and_b32_e32 v7, 0xffffff80, v6
	v_readlane_b32 s9, v255, 40
	v_add_u32_e32 v109, s13, v6
	s_add_i32 s4, 0, 0x14900
	v_mov_b32_e32 v6, s8
	s_movk_i32 s8, 0x1010
	v_lshl_add_u64 v[102:103], s[6:7], 0, v[32:33]
	s_add_i32 s6, 0, 0x1e800
	v_lshl_add_u32 v64, v5, 3, s42
	v_readlane_b32 s11, v252, 46
	v_add3_u32 v108, s9, v7, v32
	v_add_u32_e32 v110, s4, v32
	v_mad_u32_u24 v78, v4, s8, v6
	v_lshl_add_u32 v112, v95, 4, s6
	s_add_u32 s6, s10, s40
	s_addc_u32 s7, s11, s41
	v_lshlrev_b32_e32 v32, 2, v4
	v_lshlrev_b32_e32 v1, 5, v5
	v_lshlrev_b32_e32 v80, 2, v5
	v_lshl_add_u64 v[62:63], s[6:7], 0, v[32:33]
	v_add_u32_e32 v111, s13, v7
	v_readlane_b32 s6, v255, 15
	v_lshl_add_u64 v[100:101], s[36:37], 0, v[2:3]
	v_lshlrev_b64 v[2:3], 1, v[2:3]
	v_readlane_b32 s7, v255, 16
	v_readlane_b32 s14, v252, 49
	v_readlane_b32 s15, v252, 50
	v_add_u32_e32 v79, s9, v32
	s_mov_b32 s12, 0
	v_cmp_eq_u32_e64 s[4:5], 0, v106
	v_lshl_add_u32 v113, v106, 5, 0
	v_lshl_add_u64 v[104:105], s[94:95], 0, v[2:3]
	v_add_u32_e32 v114, v78, v1
	v_readlane_b32 s13, v255, 30
	v_readlane_b32 s14, v255, 19
	v_readlane_b32 s15, v252, 6
	v_readlane_b32 s16, v252, 51
	v_readlane_b32 s17, v252, 52
	v_readlane_b32 s18, v252, 53
	v_readlane_b32 s19, v252, 54
	v_readlane_b32 s20, v252, 55
	v_readlane_b32 s21, v252, 56
	v_readlane_b32 s22, v252, 57
	v_readlane_b32 s23, v252, 58
	v_lshl_add_u64 v[74:75], s[6:7], 0, v[2:3]
	v_readlane_b32 s6, v255, 28
	v_add_lshl_u32 v80, v80, s6, 7
	s_add_i32 s6, 0, 0x14a00
	v_lshl_add_u32 v32, v95, 6, s6
	v_add_u32_e32 v115, v79, v80
	v_ashrrev_i32_e32 v65, 31, v64
	v_lshlrev_b64 v[178:179], 7, v[64:65]
	s_mov_b64 s[98:99], 0x1000
	v_lshl_add_u64 v[178:179], v[62:63], 0, v[178:179]
	v_lshl_add_u64 v[180:181], v[178:179], 0, s[98:99]
	v_lshl_add_u64 v[182:183], v[180:181], 0, s[98:99]
	v_lshl_add_u64 v[184:185], v[182:183], 0, s[98:99]
	global_load_dword v4, v[184:185], off offset:64
	global_load_dword v8, v[184:185], off offset:192
	global_load_dword v5, v[184:185], off offset:320
	global_load_dword v9, v[184:185], off offset:448
	global_load_dword v6, v[184:185], off offset:576
	global_load_dword v10, v[184:185], off offset:704
	global_load_dword v7, v[184:185], off offset:832
	global_load_dword v11, v[184:185], off offset:960
	global_load_dword v12, v[184:185], off
	global_load_dword v16, v[184:185], off offset:128
	global_load_dword v13, v[184:185], off offset:256
	global_load_dword v17, v[184:185], off offset:384
	global_load_dword v14, v[184:185], off offset:512
	global_load_dword v18, v[184:185], off offset:640
	global_load_dword v15, v[184:185], off offset:768
	global_load_dword v19, v[184:185], off offset:896
	global_load_dword v20, v[182:183], off offset:64
	global_load_dword v24, v[182:183], off offset:192
	global_load_dword v21, v[182:183], off offset:320
	global_load_dword v25, v[182:183], off offset:448
	global_load_dword v22, v[182:183], off offset:576
	global_load_dword v26, v[182:183], off offset:704
	global_load_dword v23, v[182:183], off offset:832
	global_load_dword v27, v[182:183], off offset:960
	global_load_dword v28, v[182:183], off
	global_load_dword v34, v[182:183], off offset:128
	global_load_dword v29, v[182:183], off offset:256
	global_load_dword v35, v[182:183], off offset:384
; __global__ void __launch_bounds__(NWAVES * 64, 2) mk_fwd(Args args) {
;     ...
;             bf16x8 rwh[4][2], rwl[4][2];
; #pragma unroll
;             for (int ks = 0; ks < 4; ++ks)
; #pragma unroll
;                 for (int tile = 0; tile < 2; ++tile) { float f[8];
; #pragma unroll
;                     for (int j = 0; j < 8; ++j) f[j] = rw[(size_t)(128 * wave + 32 * ks + 8 * kq + j) * NEXP + 16 * tile + tk];
;                     split8(f, rwh[ks][tile], rwl[ks][tile]); }
;             int nbatch = 0;
;             for (int rep = 0; rep < NREP(3); ++rep) {
;             const bool dummy = rep + 1 < NREP(3);
;             bf16_t* XBo = dummy ? CAT : XB; unsigned char* XQo = dummy ? (unsigned char*)HB : ws + WS_XQ;
;             if (rep > 0) { __syncthreads(); if (tid < 32) LCNT[tid] = 0; __syncthreads(); }
;             nbatch = 0;
;             u32x4 yp[2][2];
;             {   const int b0 = bx < T / 16 ? bx : 0;
; #pragma unroll
;                 for (int ii = 0; ii < 2; ++ii) { const size_t t = (size_t)b0 * 16 + wave * 2 + ii; yp[ii][0] = *(const u32x4*)(YB + t * D + 8 * lane); yp[ii][1] = *(const u32x4*)(YB + t * D + 512 + 8 * lane); } }
	global_load_dword v30, v[182:183], off offset:512
	global_load_dword v36, v[182:183], off offset:640
	global_load_dword v31, v[182:183], off offset:768
	global_load_dword v37, v[182:183], off offset:896
	global_load_dword v38, v[180:181], off offset:64
	global_load_dword v42, v[180:181], off offset:192
	global_load_dword v39, v[180:181], off offset:320
	global_load_dword v43, v[180:181], off offset:448
	global_load_dword v40, v[180:181], off offset:576
	global_load_dword v44, v[180:181], off offset:704
	global_load_dword v41, v[180:181], off offset:832
	global_load_dword v45, v[180:181], off offset:960
	global_load_dword v46, v[180:181], off
	global_load_dword v50, v[180:181], off offset:128
	global_load_dword v47, v[180:181], off offset:256
	global_load_dword v51, v[180:181], off offset:384
	global_load_dword v48, v[180:181], off offset:512
	global_load_dword v52, v[180:181], off offset:640
	global_load_dword v49, v[180:181], off offset:768
	global_load_dword v53, v[180:181], off offset:896
	global_load_dword v54, v[178:179], off offset:64
	global_load_dword v58, v[178:179], off offset:192
	global_load_dword v55, v[178:179], off offset:320
	global_load_dword v59, v[178:179], off offset:448
	global_load_dword v56, v[178:179], off offset:576
	global_load_dword v60, v[178:179], off offset:704
	global_load_dword v57, v[178:179], off offset:832
	global_load_dword v61, v[178:179], off offset:960
	global_load_dword v62, v[178:179], off
	global_load_dword v66, v[178:179], off offset:128
	global_load_dword v63, v[178:179], off offset:256
	global_load_dword v67, v[178:179], off offset:384
	global_load_dword v64, v[178:179], off offset:512
	global_load_dword v68, v[178:179], off offset:640
	global_load_dword v65, v[178:179], off offset:768
	global_load_dword v69, v[178:179], off offset:896
	global_load_dwordx4 v[82:85], v[74:75], off offset:3072 nt
	global_load_dwordx4 v[78:81], v[74:75], off offset:2048 nt
	global_load_dwordx4 v[70:73], v[74:75], off offset:1024 nt
	s_nop 0
	global_load_dwordx4 v[74:77], v[74:75], off nt
	global_load_dword v249, v[102:103], off
	s_waitcnt vmcnt(61)
	v_cvt_pk_bf16_f32 v186, v4, v8
	v_cvt_pk_bf16_f32 v187, v5, v9
	v_cvt_pk_bf16_f32 v188, v6, v10
	v_cvt_pk_bf16_f32 v189, v7, v11
	v_lshlrev_b32_e32 v190, 16, v186
	v_and_b32_e32 v194, 0xffff0000, v186
	v_lshlrev_b32_e32 v191, 16, v187
	v_and_b32_e32 v195, 0xffff0000, v187
	v_lshlrev_b32_e32 v192, 16, v188
	v_and_b32_e32 v196, 0xffff0000, v188
	v_lshlrev_b32_e32 v193, 16, v189
	v_and_b32_e32 v197, 0xffff0000, v189
	v_sub_f32_e32 v4, v4, v190
	v_sub_f32_e32 v8, v8, v194
	v_sub_f32_e32 v5, v5, v191
	v_sub_f32_e32 v9, v9, v195
	v_sub_f32_e32 v6, v6, v192
	v_sub_f32_e32 v10, v10, v196
	v_sub_f32_e32 v7, v7, v193
	v_sub_f32_e32 v11, v11, v197
	v_cvt_pk_bf16_f32 v8, v4, v8
	v_cvt_pk_bf16_f32 v9, v5, v9
	v_cvt_pk_bf16_f32 v10, v6, v10
	v_cvt_pk_bf16_f32 v11, v7, v11
	v_mov_b32_e32 v4, v186
	v_mov_b32_e32 v5, v187
	v_mov_b32_e32 v6, v188
	v_mov_b32_e32 v7, v189
	s_waitcnt vmcnt(53)
	v_cvt_pk_bf16_f32 v186, v12, v16
	v_cvt_pk_bf16_f32 v187, v13, v17
	v_cvt_pk_bf16_f32 v188, v14, v18
	v_cvt_pk_bf16_f32 v189, v15, v19
	v_lshlrev_b32_e32 v190, 16, v186
	v_and_b32_e32 v194, 0xffff0000, v186
	v_lshlrev_b32_e32 v191, 16, v187
	v_and_b32_e32 v195, 0xffff0000, v187
	v_lshlrev_b32_e32 v192, 16, v188
	v_and_b32_e32 v196, 0xffff0000, v188
	v_lshlrev_b32_e32 v193, 16, v189
	v_and_b32_e32 v197, 0xffff0000, v189
	v_sub_f32_e32 v12, v12, v190
	v_sub_f32_e32 v16, v16, v194
	v_sub_f32_e32 v13, v13, v191
	v_sub_f32_e32 v17, v17, v195
	v_sub_f32_e32 v14, v14, v192
	v_sub_f32_e32 v18, v18, v196
	v_sub_f32_e32 v15, v15, v193
	v_sub_f32_e32 v19, v19, v197
	v_cvt_pk_bf16_f32 v16, v12, v16
	v_cvt_pk_bf16_f32 v17, v13, v17
	v_cvt_pk_bf16_f32 v18, v14, v18
	v_cvt_pk_bf16_f32 v19, v15, v19
	v_mov_b32_e32 v12, v186
	v_mov_b32_e32 v13, v187
	v_mov_b32_e32 v14, v188
	v_mov_b32_e32 v15, v189
	s_waitcnt vmcnt(45)
	v_cvt_pk_bf16_f32 v186, v20, v24
	v_cvt_pk_bf16_f32 v187, v21, v25
	v_cvt_pk_bf16_f32 v188, v22, v26
	v_cvt_pk_bf16_f32 v189, v23, v27
	v_lshlrev_b32_e32 v190, 16, v186
	v_and_b32_e32 v194, 0xffff0000, v186
	v_lshlrev_b32_e32 v191, 16, v187
	v_and_b32_e32 v195, 0xffff0000, v187
	v_lshlrev_b32_e32 v192, 16, v188
	v_and_b32_e32 v196, 0xffff0000, v188
	v_lshlrev_b32_e32 v193, 16, v189
	v_and_b32_e32 v197, 0xffff0000, v189
	v_sub_f32_e32 v20, v20, v190
	v_sub_f32_e32 v24, v24, v194
	v_sub_f32_e32 v21, v21, v191
	v_sub_f32_e32 v25, v25, v195
	v_sub_f32_e32 v22, v22, v192
	v_sub_f32_e32 v26, v26, v196
	v_sub_f32_e32 v23, v23, v193
	v_sub_f32_e32 v27, v27, v197
	v_cvt_pk_bf16_f32 v24, v20, v24
	v_cvt_pk_bf16_f32 v25, v21, v25
	v_cvt_pk_bf16_f32 v26, v22, v26
	v_cvt_pk_bf16_f32 v27, v23, v27
	v_mov_b32_e32 v20, v186
	v_mov_b32_e32 v21, v187
	v_mov_b32_e32 v22, v188
	v_mov_b32_e32 v23, v189
	s_waitcnt vmcnt(37)
	v_cvt_pk_bf16_f32 v186, v28, v34
	v_cvt_pk_bf16_f32 v187, v29, v35
	v_cvt_pk_bf16_f32 v188, v30, v36
	v_cvt_pk_bf16_f32 v189, v31, v37
	v_lshlrev_b32_e32 v190, 16, v186
	v_and_b32_e32 v194, 0xffff0000, v186
	v_lshlrev_b32_e32 v191, 16, v187
	v_and_b32_e32 v195, 0xffff0000, v187
	v_lshlrev_b32_e32 v192, 16, v188
	v_and_b32_e32 v196, 0xffff0000, v188
	v_lshlrev_b32_e32 v193, 16, v189
	v_and_b32_e32 v197, 0xffff0000, v189
	v_sub_f32_e32 v28, v28, v190
	v_sub_f32_e32 v34, v34, v194
	v_sub_f32_e32 v29, v29, v191
	v_sub_f32_e32 v35, v35, v195
	v_sub_f32_e32 v30, v30, v192
	v_sub_f32_e32 v36, v36, v196
	v_sub_f32_e32 v31, v31, v193
	v_sub_f32_e32 v37, v37, v197
	v_cvt_pk_bf16_f32 v34, v28, v34
	v_cvt_pk_bf16_f32 v35, v29, v35
	v_cvt_pk_bf16_f32 v36, v30, v36
	v_cvt_pk_bf16_f32 v37, v31, v37
	v_mov_b32_e32 v28, v186
	v_mov_b32_e32 v29, v187
	v_mov_b32_e32 v30, v188
	v_mov_b32_e32 v31, v189
	s_waitcnt vmcnt(29)
; __device__ __forceinline__ void unpack8(const u32x4 w, float (&f)[8]) { f[0] = bf_lo(w.x); f[1] = bf_hi(w.x); f[2] = bf_lo(w.y); f[3] = bf_hi(w.y); f[4] = bf_lo(w.z); f[5] = bf_hi(w.z); f[6] = bf_lo(w.w); f[7] = bf_hi(w.w); }
; __device__ __forceinline__ u32x4 pack8(const float (&f)[8]) { u32x4 o; o.x = cvt_pk_bf16(f[0], f[1]); o.y = cvt_pk_bf16(f[2], f[3]); o.z = cvt_pk_bf16(f[4], f[5]); o.w = cvt_pk_bf16(f[6], f[7]); return o; }
; __global__ void __launch_bounds__(NWAVES * 64, 2) mk_fwd(Args args) {
;     ...
;             auto split8 = [](const float (&f)[8], bf16x8& hi, bf16x8& lo) { const u32x4 h = pack8(f); float fh[8], fl[8]; unpack8(h, fh);
; #pragma unroll
;                 for (int i = 0; i < 8; ++i) fl[i] = f[i] - fh[i];
;                 hi = __builtin_bit_cast(bf16x8, h); lo = __builtin_bit_cast(bf16x8, pack8(fl)); };
;             bf16x8 rwh[4][2], rwl[4][2];
; #pragma unroll
;             for (int ks = 0; ks < 4; ++ks)
; #pragma unroll
;                 for (int tile = 0; tile < 2; ++tile) { float f[8];
; #pragma unroll
;                     for (int j = 0; j < 8; ++j) f[j] = rw[(size_t)(128 * wave + 32 * ks + 8 * kq + j) * NEXP + 16 * tile + tk];
;                     split8(f, rwh[ks][tile], rwl[ks][tile]); }
;     ...
;             for (int bi = bx; bi < T / 16; bi += G, ++nbatch) {
;                 u32x4 yc[2][2];
; #pragma unroll
;                 for (int ii = 0; ii < 2; ++ii) { yc[ii][0] = yp[ii][0]; yc[ii][1] = yp[ii][1]; }
;                 {   const int bn = (bi + G < T / 16) ? bi + G : bi;
; #pragma unroll
;                     for (int ii = 0; ii < 2; ++ii) { const size_t t = (size_t)bn * 16 + wave * 2 + ii; yp[ii][0] = *(const u32x4*)(YB + t * D + 8 * lane); yp[ii][1] = *(const u32x4*)(YB + t * D + 512 + 8 * lane); } }
; #pragma unroll
;                 for (int ii = 0; ii < 2; ++ii) {
;                     const int tl = wave * 2 + ii, t = bi * 16 + tl;
;                     float v[16], o[16];
; #pragma unroll
;                     for (int hf = 0; hf < 2; ++hf) { float f[8]; unpack8(yc[ii][hf], f);
; #pragma unroll
;                         for (int i = 0; i < 8; ++i) v[8 * hf + i] = f[i]; }
;                     ln_row16(v, lng, lnb, lane, o);
	v_cvt_pk_bf16_f32 v186, v38, v42
	v_cvt_pk_bf16_f32 v187, v39, v43
	v_cvt_pk_bf16_f32 v188, v40, v44
	v_cvt_pk_bf16_f32 v189, v41, v45
	v_lshlrev_b32_e32 v190, 16, v186
	v_and_b32_e32 v194, 0xffff0000, v186
	v_lshlrev_b32_e32 v191, 16, v187
	v_and_b32_e32 v195, 0xffff0000, v187
	v_lshlrev_b32_e32 v192, 16, v188
	v_and_b32_e32 v196, 0xffff0000, v188
	v_lshlrev_b32_e32 v193, 16, v189
	v_and_b32_e32 v197, 0xffff0000, v189
	v_sub_f32_e32 v38, v38, v190
	v_sub_f32_e32 v42, v42, v194
	v_sub_f32_e32 v39, v39, v191
	v_sub_f32_e32 v43, v43, v195
	v_sub_f32_e32 v40, v40, v192
	v_sub_f32_e32 v44, v44, v196
	v_sub_f32_e32 v41, v41, v193
	v_sub_f32_e32 v45, v45, v197
	v_cvt_pk_bf16_f32 v42, v38, v42
	v_cvt_pk_bf16_f32 v43, v39, v43
	v_cvt_pk_bf16_f32 v44, v40, v44
	v_cvt_pk_bf16_f32 v45, v41, v45
	v_mov_b32_e32 v38, v186
	v_mov_b32_e32 v39, v187
	v_mov_b32_e32 v40, v188
	v_mov_b32_e32 v41, v189
	s_waitcnt vmcnt(21)
	v_cvt_pk_bf16_f32 v186, v46, v50
	v_cvt_pk_bf16_f32 v187, v47, v51
	v_cvt_pk_bf16_f32 v188, v48, v52
	v_cvt_pk_bf16_f32 v189, v49, v53
	v_lshlrev_b32_e32 v190, 16, v186
	v_and_b32_e32 v194, 0xffff0000, v186
	v_lshlrev_b32_e32 v191, 16, v187
	v_and_b32_e32 v195, 0xffff0000, v187
	v_lshlrev_b32_e32 v192, 16, v188
	v_and_b32_e32 v196, 0xffff0000, v188
	v_lshlrev_b32_e32 v193, 16, v189
	v_and_b32_e32 v197, 0xffff0000, v189
	v_sub_f32_e32 v46, v46, v190
	v_sub_f32_e32 v50, v50, v194
	v_sub_f32_e32 v47, v47, v191
	v_sub_f32_e32 v51, v51, v195
	v_sub_f32_e32 v48, v48, v192
	v_sub_f32_e32 v52, v52, v196
	v_sub_f32_e32 v49, v49, v193
	v_sub_f32_e32 v53, v53, v197
	v_cvt_pk_bf16_f32 v50, v46, v50
	v_cvt_pk_bf16_f32 v51, v47, v51
	v_cvt_pk_bf16_f32 v52, v48, v52
	v_cvt_pk_bf16_f32 v53, v49, v53
	v_mov_b32_e32 v46, v186
	v_mov_b32_e32 v47, v187
	v_mov_b32_e32 v48, v188
	v_mov_b32_e32 v49, v189
	s_waitcnt vmcnt(13)
	v_cvt_pk_bf16_f32 v186, v54, v58
	v_cvt_pk_bf16_f32 v187, v55, v59
	v_cvt_pk_bf16_f32 v188, v56, v60
	v_cvt_pk_bf16_f32 v189, v57, v61
	v_lshlrev_b32_e32 v190, 16, v186
	v_and_b32_e32 v194, 0xffff0000, v186
	v_lshlrev_b32_e32 v191, 16, v187
	v_and_b32_e32 v195, 0xffff0000, v187
	v_lshlrev_b32_e32 v192, 16, v188
	v_and_b32_e32 v196, 0xffff0000, v188
	v_lshlrev_b32_e32 v193, 16, v189
	v_and_b32_e32 v197, 0xffff0000, v189
	v_sub_f32_e32 v54, v54, v190
	v_sub_f32_e32 v58, v58, v194
	v_sub_f32_e32 v55, v55, v191
	v_sub_f32_e32 v59, v59, v195
	v_sub_f32_e32 v56, v56, v192
	v_sub_f32_e32 v60, v60, v196
	v_sub_f32_e32 v57, v57, v193
	v_sub_f32_e32 v61, v61, v197
	v_cvt_pk_bf16_f32 v58, v54, v58
	v_cvt_pk_bf16_f32 v59, v55, v59
	v_cvt_pk_bf16_f32 v60, v56, v60
	v_cvt_pk_bf16_f32 v61, v57, v61
	v_mov_b32_e32 v54, v186
	v_mov_b32_e32 v55, v187
	v_mov_b32_e32 v56, v188
	v_mov_b32_e32 v57, v189
	s_waitcnt vmcnt(5)
	v_cvt_pk_bf16_f32 v186, v62, v66
	v_cvt_pk_bf16_f32 v187, v63, v67
	v_cvt_pk_bf16_f32 v188, v64, v68
	v_cvt_pk_bf16_f32 v189, v65, v69
	v_lshlrev_b32_e32 v190, 16, v186
	v_and_b32_e32 v194, 0xffff0000, v186
	v_lshlrev_b32_e32 v191, 16, v187
	v_and_b32_e32 v195, 0xffff0000, v187
	v_lshlrev_b32_e32 v192, 16, v188
	v_and_b32_e32 v196, 0xffff0000, v188
	v_lshlrev_b32_e32 v193, 16, v189
	v_and_b32_e32 v197, 0xffff0000, v189
	v_sub_f32_e32 v62, v62, v190
	v_sub_f32_e32 v66, v66, v194
	v_sub_f32_e32 v63, v63, v191
	v_sub_f32_e32 v67, v67, v195
	v_sub_f32_e32 v64, v64, v192
	v_sub_f32_e32 v68, v68, v196
	v_sub_f32_e32 v65, v65, v193
	v_sub_f32_e32 v69, v69, v197
	v_cvt_pk_bf16_f32 v66, v62, v66
	v_cvt_pk_bf16_f32 v67, v63, v67
	v_cvt_pk_bf16_f32 v68, v64, v68
	v_cvt_pk_bf16_f32 v69, v65, v69
	v_mov_b32_e32 v62, v186
	v_mov_b32_e32 v63, v187
	v_mov_b32_e32 v64, v188
	v_mov_b32_e32 v65, v189
.LBB0_485:
	s_mov_b32 s6, s15
	s_add_i32 s15, s15, s72
	s_cmpk_gt_i32 s15, 0x7ff
	s_cselect_b64 s[8:9], -1, 0
	s_cmpk_lt_i32 s15, 0x800
	s_cselect_b32 s6, s15, s6
	s_ashr_i32 s7, s6, 31
	s_lshl_b64 s[6:7], s[6:7], 4
	v_readlane_b32 s10, v255, 19
	s_add_u32 s6, s6, s10
	s_addc_u32 s7, s7, 0
	s_lshl_b64 s[6:7], s[6:7], 11
	s_mov_b64 s[98:99], s[6:7]
	s_waitcnt vmcnt(0)
	v_mov_b64_e32 v[88:89], v[84:85]
	v_mov_b64_e32 v[92:93], v[80:81]
	v_mov_b64_e32 v[86:87], v[82:83]
	v_mov_b64_e32 v[90:91], v[78:79]
	v_mov_b64_e32 v[118:119], v[76:77]
	v_mov_b64_e32 v[122:123], v[72:73]
	v_mov_b64_e32 v[116:117], v[74:75]
	v_mov_b64_e32 v[120:121], v[70:71]
	global_load_dwordx4 v[124:127], v[96:97], off offset:16
	global_load_dwordx4 v[128:131], v[96:97], off
	global_load_dwordx4 v[132:135], v[98:99], off offset:16
	global_load_dwordx4 v[136:139], v[98:99], off
	v_lshlrev_b32_e32 v2, 16, v116
	v_and_b32_e32 v3, 0xffff0000, v116
	v_lshlrev_b32_e32 v152, 16, v117
	v_and_b32_e32 v153, 0xffff0000, v117
	v_lshlrev_b32_e32 v154, 16, v118
	v_and_b32_e32 v155, 0xffff0000, v118
	v_lshlrev_b32_e32 v156, 16, v119
	v_and_b32_e32 v157, 0xffff0000, v119
	global_load_dwordx4 v[116:119], v[96:97], off offset:2064
	global_load_dwordx4 v[140:143], v[96:97], off offset:2048
	global_load_dwordx4 v[144:147], v[98:99], off offset:2064
	global_load_dwordx4 v[148:151], v[98:99], off offset:2048
	v_lshlrev_b32_e32 v160, 16, v122
	v_and_b32_e32 v161, 0xffff0000, v122
	v_lshlrev_b32_e32 v122, 16, v123
	v_and_b32_e32 v123, 0xffff0000, v123
	v_lshlrev_b32_e32 v158, 16, v120
	v_and_b32_e32 v159, 0xffff0000, v120
	v_lshlrev_b32_e32 v120, 16, v121
	v_and_b32_e32 v121, 0xffff0000, v121
	v_add_f32_e32 v1, v123, v122
	v_add_f32_e32 v162, v161, v160
	v_add_f32_e32 v1, v162, v1
	v_add_f32_e32 v162, v121, v120
	v_add_f32_e32 v163, v159, v158
	v_add_f32_e32 v162, v163, v162
	v_add_f32_e32 v1, v162, v1
	v_add_f32_e32 v162, v157, v156
	v_add_f32_e32 v163, v155, v154
	v_add_f32_e32 v162, v163, v162
	v_add_f32_e32 v163, v153, v152
	v_add_f32_e32 v164, v3, v2
	v_add_f32_e32 v163, v164, v163
	v_add_f32_e32 v162, v163, v162
	v_add_f32_e32 v1, v162, v1
	s_mov_b32 s6, 0xf800000
	s_nop 0
	v_add_f32_dpp v1, v1, v1 quad_perm:[1,0,3,2] row_mask:0xf bank_mask:0xf bound_ctrl:1
	s_nop 1
	v_add_f32_dpp v1, v1, v1 quad_perm:[2,3,0,1] row_mask:0xf bank_mask:0xf bound_ctrl:1
	s_nop 1
	v_add_f32_dpp v1, v1, v1 row_half_mirror row_mask:0xf bank_mask:0xf bound_ctrl:1
	s_nop 1
	v_add_f32_dpp v1, v1, v1 row_mirror row_mask:0xf bank_mask:0xf bound_ctrl:1
	ds_swizzle_b32 v162, v1 offset:swizzle(SWAP,16)
	s_waitcnt lgkmcnt(0)
; #define LAS __attribute__((address_space(3)))
; __device__ __forceinline__ float wave_sum(float v) { v += dpp_f<0xB1>(v); v += dpp_f<0x4E>(v); v += dpp_f<0x141>(v); v += dpp_f<0x140>(v); v += xor_sw<16>(v); return sum_x32(v); }
; __device__ __forceinline__ float wave_max(float v) { v = fmaxf(v, dpp_f<0xB1>(v)); v = fmaxf(v, dpp_f<0x4E>(v)); v = fmaxf(v, dpp_f<0x141>(v)); v = fmaxf(v, dpp_f<0x140>(v)); v = fmaxf(v, xor_sw<16>(v)); return max_x32(v); }
; __device__ __forceinline__ void ln_row16(float (&v)[16], const float* lng, const float* lnb, int lane, float (&o)[16]) {
;     const float s = ((v[0] + v[1]) + (v[2] + v[3])) + ((v[4] + v[5]) + (v[6] + v[7])) + (((v[8] + v[9]) + (v[10] + v[11])) + ((v[12] + v[13]) + (v[14] + v[15])));
;     const float mean = wave_sum(s) * (1.0f / D);
; #pragma unroll
;     for (int i = 0; i < 16; ++i) v[i] -= mean;
;     const float s2 = ((v[0] * v[0] + v[1] * v[1]) + (v[2] * v[2] + v[3] * v[3])) + ((v[4] * v[4] + v[5] * v[5]) + (v[6] * v[6] + v[7] * v[7]))
;                    + (((v[8] * v[8] + v[9] * v[9]) + (v[10] * v[10] + v[11] * v[11])) + ((v[12] * v[12] + v[13] * v[13]) + (v[14] * v[14] + v[15] * v[15])));
;     const float rstd = 1.0f / sqrtf(wave_sum(s2) * (1.0f / D) + LN_EPS);
; #pragma unroll
;     for (int hf = 0; hf < 2; ++hf) { const int col = 512 * hf + 8 * lane;
;         const f32x4 g0 = *(const f32x4*)(lng + col), g1 = *(const f32x4*)(lng + col + 4), b0 = *(const f32x4*)(lnb + col), b1 = *(const f32x4*)(lnb + col + 4);
; #pragma unroll
;         for (int i = 0; i < 4; ++i) { o[8 * hf + i] = v[8 * hf + i] * rstd * g0[i] + b0[i]; o[8 * hf + 4 + i] = v[8 * hf + 4 + i] * rstd * g1[i] + b1[i]; } }
; }
; __device__ __forceinline__ float q8_row16(const float (&o)[16], unsigned char* qrow, int lane) {
;     float am = 0.f;
; #pragma unroll
;     for (int i = 0; i < 16; ++i) am = fmaxf(am, fabsf(o[i]));
;     am = wave_max(am);
; __global__ void __launch_bounds__(NWAVES * 64, 2) mk_fwd(Args args) {
;     ...
;                     for (int hf = 0; hf < 2; ++hf) { const int col = 512 * hf + 8 * lane;
;                         *(LAS f32x4*)(XL + tl * XS + col) = (f32x4){o[8 * hf], o[8 * hf + 1], o[8 * hf + 2], o[8 * hf + 3]}; *(LAS f32x4*)(XL + tl * XS + col + 4) = (f32x4){o[8 * hf + 4], o[8 * hf + 5], o[8 * hf + 6], o[8 * hf + 7]}; }
	v_add_f32_e32 v1, v1, v162
	v_mov_b32_e32 v162, v1
	s_nop 1
	v_permlane32_swap_b32_e32 v1, v162
	v_add_f32_e32 v1, v1, v162
	v_mul_f32_e32 v162, 0x3a800000, v1
	v_pk_add_f32 v[2:3], v[2:3], v[162:163] op_sel_hi:[1,0] neg_lo:[0,1] neg_hi:[0,1]
	v_pk_add_f32 v[152:153], v[152:153], v[162:163] op_sel_hi:[1,0] neg_lo:[0,1] neg_hi:[0,1]
	v_pk_add_f32 v[154:155], v[154:155], v[162:163] op_sel_hi:[1,0] neg_lo:[0,1] neg_hi:[0,1]
	v_pk_add_f32 v[156:157], v[156:157], v[162:163] op_sel_hi:[1,0] neg_lo:[0,1] neg_hi:[0,1]
	v_pk_add_f32 v[158:159], v[158:159], v[162:163] op_sel_hi:[1,0] neg_lo:[0,1] neg_hi:[0,1]
	v_pk_add_f32 v[164:165], v[120:121], v[162:163] op_sel_hi:[1,0] neg_lo:[0,1] neg_hi:[0,1]
	v_pk_add_f32 v[160:161], v[160:161], v[162:163] op_sel_hi:[1,0] neg_lo:[0,1] neg_hi:[0,1]
	v_pk_add_f32 v[162:163], v[122:123], v[162:163] op_sel_hi:[1,0] neg_lo:[0,1] neg_hi:[0,1]
	v_pk_mul_f32 v[120:121], v[2:3], v[2:3]
	v_pk_mul_f32 v[122:123], v[152:153], v[152:153]
	v_pk_mul_f32 v[166:167], v[154:155], v[154:155]
	v_pk_mul_f32 v[168:169], v[156:157], v[156:157]
	v_pk_mul_f32 v[170:171], v[158:159], v[158:159]
	v_pk_mul_f32 v[172:173], v[164:165], v[164:165]
	v_pk_mul_f32 v[174:175], v[160:161], v[160:161]
	v_pk_mul_f32 v[176:177], v[162:163], v[162:163]
	v_add_f32_e32 v174, v174, v175
	v_add_f32_e32 v1, v176, v177
	v_add_f32_e32 v172, v172, v173
	v_add_f32_e32 v170, v170, v171
	v_add_f32_e32 v168, v168, v169
	v_add_f32_e32 v166, v166, v167
	v_add_f32_e32 v122, v122, v123
	v_add_f32_e32 v120, v120, v121
	v_add_f32_e32 v1, v174, v1
	v_add_f32_e32 v170, v170, v172
	v_add_f32_e32 v166, v166, v168
	v_add_f32_e32 v120, v120, v122
	v_add_f32_e32 v1, v170, v1
	v_add_f32_e32 v120, v120, v166
	v_add_f32_e32 v1, v120, v1
	s_nop 1
	v_add_f32_dpp v1, v1, v1 quad_perm:[1,0,3,2] row_mask:0xf bank_mask:0xf bound_ctrl:1
	s_nop 1
	v_add_f32_dpp v1, v1, v1 quad_perm:[2,3,0,1] row_mask:0xf bank_mask:0xf bound_ctrl:1
	s_nop 1
	v_add_f32_dpp v1, v1, v1 row_half_mirror row_mask:0xf bank_mask:0xf bound_ctrl:1
	s_nop 1
	v_add_f32_dpp v1, v1, v1 row_mirror row_mask:0xf bank_mask:0xf bound_ctrl:1
	ds_swizzle_b32 v120, v1 offset:swizzle(SWAP,16)
	s_waitcnt lgkmcnt(0)
	v_add_f32_e32 v1, v1, v120
	v_mov_b32_e32 v120, v1
	s_nop 1
	v_permlane32_swap_b32_e32 v1, v120
	v_add_f32_e32 v1, v1, v120
	v_fmamk_f32 v1, v1, 0x3a800000, v250
	v_cmp_gt_f32_e32 vcc, s6, v1
	v_mul_f32_e32 v120, 0x4f800000, v1
	s_nop 0
	v_cndmask_b32_e32 v1, v1, v120, vcc
	v_sqrt_f32_e32 v120, v1
	s_nop 0
	v_add_u32_e32 v121, -1, v120
	v_fma_f32 v122, -v121, v120, v1
	v_cmp_ge_f32_e64 s[6:7], 0, v122
	v_add_u32_e32 v122, 1, v120
	s_nop 0
	v_cndmask_b32_e64 v121, v120, v121, s[6:7]
	v_fma_f32 v120, -v122, v120, v1
	v_cmp_lt_f32_e64 s[6:7], 0, v120
	s_nop 1
	v_cndmask_b32_e64 v120, v121, v122, s[6:7]
	v_mul_f32_e32 v121, 0x37800000, v120
	v_cndmask_b32_e32 v120, v120, v121, vcc
	v_cmp_class_f32_e32 vcc, v1, v251
	s_nop 1
	v_cndmask_b32_e32 v1, v120, v1, vcc
	v_div_scale_f32 v120, s[6:7], v1, v1, 1.0
	v_rcp_f32_e32 v121, v120
	s_mul_i32 s6, s73, 0x2020
	v_fma_f32 v122, -v120, v121, 1.0
	v_fmac_f32_e32 v121, v122, v121
	v_div_scale_f32 v122, vcc, 1.0, v1, 1.0
	v_mul_f32_e32 v123, v122, v121
	v_fma_f32 v166, -v120, v123, v122
	v_fmac_f32_e32 v123, v166, v121
	v_fma_f32 v120, -v120, v123, v122
	v_div_fmas_f32 v120, v120, v121, v123
	v_div_fixup_f32 v166, v120, v1, 1.0
	v_pk_mul_f32 v[2:3], v[2:3], v[166:167] op_sel_hi:[1,0]
	v_add_u32_e32 v1, s6, v113
	s_waitcnt vmcnt(4)
	v_pk_fma_f32 v[120:121], v[128:129], v[2:3], v[136:137]
	v_pk_mul_f32 v[2:3], v[154:155], v[166:167] op_sel_hi:[1,0]
	v_readlane_b32 s6, v255, 36
	v_pk_fma_f32 v[124:125], v[124:125], v[2:3], v[132:133]
	v_pk_mul_f32 v[2:3], v[152:153], v[166:167] op_sel_hi:[1,0]
	s_add_i32 s10, s6, s14
	v_pk_fma_f32 v[122:123], v[130:131], v[2:3], v[138:139]
	v_pk_mul_f32 v[2:3], v[156:157], v[166:167] op_sel_hi:[1,0]
	s_ashr_i32 s11, s10, 31
	v_pk_fma_f32 v[126:127], v[126:127], v[2:3], v[134:135]
	v_pk_mul_f32 v[2:3], v[158:159], v[166:167] op_sel_hi:[1,0]
	s_lshl_b64 s[6:7], s[10:11], 10
	s_waitcnt vmcnt(0)
	v_pk_fma_f32 v[128:129], v[140:141], v[2:3], v[148:149]
	v_pk_mul_f32 v[2:3], v[160:161], v[166:167] op_sel_hi:[1,0]
	s_nop 0
	v_pk_fma_f32 v[116:117], v[116:117], v[2:3], v[144:145]
	v_pk_mul_f32 v[2:3], v[164:165], v[166:167] op_sel_hi:[1,0]
	s_nop 0
	v_pk_fma_f32 v[130:131], v[142:143], v[2:3], v[150:151]
	v_pk_mul_f32 v[2:3], v[162:163], v[166:167] op_sel_hi:[1,0]
	s_nop 0
	v_pk_fma_f32 v[118:119], v[118:119], v[2:3], v[146:147]
	ds_write_b128 v1, v[120:123]
	ds_write_b128 v1, v[124:127] offset:16
	ds_write_b128 v1, v[128:131] offset:2048
	ds_write_b128 v1, v[116:119] offset:2064
	v_max3_f32 v1, |v120|, 0, |v121|
	v_max3_f32 v1, v1, |v122|, |v123|
	v_max3_f32 v1, v1, |v124|, |v125|
	v_max3_f32 v1, v1, |v126|, |v127|
	v_max3_f32 v1, v1, |v128|, |v129|
	v_max3_f32 v1, v1, |v130|, |v131|
	v_max3_f32 v1, v1, |v116|, |v117|
	v_max3_f32 v1, v1, |v118|, |v119|
	s_nop 1
	v_mov_b32_dpp v2, v1 quad_perm:[1,0,3,2] row_mask:0xf bank_mask:0xf bound_ctrl:1
	v_max_f32_e32 v2, v2, v2
	v_max_f32_e32 v1, v1, v2
	s_nop 1
	v_mov_b32_dpp v2, v1 quad_perm:[2,3,0,1] row_mask:0xf bank_mask:0xf bound_ctrl:1
	v_max_f32_e32 v2, v2, v2
	v_max_f32_e32 v1, v1, v2
	s_nop 1
	v_mov_b32_dpp v2, v1 row_half_mirror row_mask:0xf bank_mask:0xf bound_ctrl:1
	v_max_f32_e32 v2, v2, v2
	v_max_f32_e32 v1, v1, v2
	s_nop 1
	v_mov_b32_dpp v2, v1 row_mirror row_mask:0xf bank_mask:0xf bound_ctrl:1
	v_max_f32_e32 v2, v2, v2
	v_max_f32_e32 v1, v1, v2
	ds_swizzle_b32 v2, v1 offset:swizzle(SWAP,16)
	s_waitcnt lgkmcnt(0)
; #define LAS __attribute__((address_space(3)))
; __device__ __forceinline__ void unpack8(const u32x4 w, float (&f)[8]) { f[0] = bf_lo(w.x); f[1] = bf_hi(w.x); f[2] = bf_lo(w.y); f[3] = bf_hi(w.y); f[4] = bf_lo(w.z); f[5] = bf_hi(w.z); f[6] = bf_lo(w.w); f[7] = bf_hi(w.w); }
; __device__ __forceinline__ float wave_max(float v) { v = fmaxf(v, dpp_f<0xB1>(v)); v = fmaxf(v, dpp_f<0x4E>(v)); v = fmaxf(v, dpp_f<0x141>(v)); v = fmaxf(v, dpp_f<0x140>(v)); v = fmaxf(v, xor_sw<16>(v)); return max_x32(v); }
; __device__ __forceinline__ float q8_row16(const float (&o)[16], unsigned char* qrow, int lane) {
;     float am = 0.f;
; #pragma unroll
;     for (int i = 0; i < 16; ++i) am = fmaxf(am, fabsf(o[i]));
;     am = wave_max(am);
;     const float qs = am > 0.f ? am * (1.0f / 127.0f) : 1.0f, qinv = 1.0f / qs;
; #pragma unroll
;     for (int hf = 0; hf < 2; ++hf) { u32x2 q; q.x = q8x4(o[8 * hf], o[8 * hf + 1], o[8 * hf + 2], o[8 * hf + 3], qinv); q.y = q8x4(o[8 * hf + 4], o[8 * hf + 5], o[8 * hf + 6], o[8 * hf + 7], qinv);
;         *(u32x2*)(qrow + 512 * hf + 8 * lane) = q; }
;     return qs;
; __global__ void __launch_bounds__(NWAVES * 64, 2) mk_fwd(Args args) {
;     ...
;                     for (int hf = 0; hf < 2; ++hf) { float f[8]; unpack8(yc[ii][hf], f);
; #pragma unroll
;                         for (int i = 0; i < 8; ++i) v[8 * hf + i] = f[i]; }
;                     ln_row16(v, lng, lnb, lane, o);
; #pragma unroll
;                     for (int hf = 0; hf < 2; ++hf) { const int col = 512 * hf + 8 * lane;
;                         *(LAS f32x4*)(XL + tl * XS + col) = (f32x4){o[8 * hf], o[8 * hf + 1], o[8 * hf + 2], o[8 * hf + 3]}; *(LAS f32x4*)(XL + tl * XS + col + 4) = (f32x4){o[8 * hf + 4], o[8 * hf + 5], o[8 * hf + 6], o[8 * hf + 7]}; }
;                     const float qs = q8_row16(o, XQo + (size_t)t * D, lane);
;                     if (lane == 0) TSC[nbatch * 16 + tl] = qs;
	v_max_f32_e32 v2, v2, v2
	v_max_f32_e32 v1, v1, v2
	v_mov_b32_e32 v2, v1
	s_nop 1
	v_permlane32_swap_b32_e32 v1, v2
	v_max_f32_e32 v2, v2, v2
	v_max_f32_e32 v1, v1, v1
	v_max_f32_e32 v1, v1, v2
	v_cmp_lt_f32_e32 vcc, 0, v1
	v_mul_f32_e32 v1, 0x3c010204, v1
	s_nop 0
	v_cndmask_b32_e32 v1, 1.0, v1, vcc
	v_div_scale_f32 v2, s[16:17], v1, v1, 1.0
	v_rcp_f32_e32 v3, v2
	s_nop 0
	v_fma_f32 v132, -v2, v3, 1.0
	v_fmac_f32_e32 v3, v132, v3
	v_div_scale_f32 v132, vcc, 1.0, v1, 1.0
	v_mul_f32_e32 v133, v132, v3
	v_fma_f32 v134, -v2, v133, v132
	v_fmac_f32_e32 v133, v134, v3
	v_fma_f32 v2, -v2, v133, v132
	v_div_fmas_f32 v2, v2, v3, v133
	v_div_fixup_f32 v132, v2, v1, 1.0
	v_fmaak_f32 v120, v120, v132, 0x4b400000
	v_fmaak_f32 v121, v121, v132, 0x4b400000
	v_fmaak_f32 v122, v122, v132, 0x4b400000
	v_fmaak_f32 v123, v123, v132, 0x4b400000
	v_perm_b32 v122, v123, v122, s61
	v_perm_b32 v120, v121, v120, s61
	v_perm_b32 v120, v122, v120, s79
	v_fmaak_f32 v121, v124, v132, 0x4b400000
	v_fmaak_f32 v122, v125, v132, 0x4b400000
	v_fmaak_f32 v123, v126, v132, 0x4b400000
	v_fmaak_f32 v124, v127, v132, 0x4b400000
	v_perm_b32 v123, v124, v123, s61
	v_perm_b32 v121, v122, v121, s61
	v_lshl_add_u64 v[2:3], v[100:101], 0, s[6:7]
	v_perm_b32 v121, v123, v121, s79
	global_store_dwordx2 v[2:3], v[120:121], off
	v_fmaak_f32 v120, v128, v132, 0x4b400000
	v_fmaak_f32 v121, v129, v132, 0x4b400000
	v_fmaak_f32 v122, v130, v132, 0x4b400000
	v_fmaak_f32 v123, v131, v132, 0x4b400000
	v_fmaak_f32 v116, v116, v132, 0x4b400000
	v_fmaak_f32 v117, v117, v132, 0x4b400000
	v_fmaak_f32 v118, v118, v132, 0x4b400000
	v_fmaak_f32 v119, v119, v132, 0x4b400000
	v_perm_b32 v122, v123, v122, s61
	v_perm_b32 v120, v121, v120, s61
	v_perm_b32 v118, v119, v118, s61
	v_perm_b32 v116, v117, v116, s61
	v_perm_b32 v120, v122, v120, s79
	v_perm_b32 v121, v118, v116, s79
	global_store_dwordx2 v[2:3], v[120:121], off offset:512
	s_and_saveexec_b64 s[6:7], s[4:5]
	s_add_i32 s11, s13, -4
	v_mov_b32_e32 v2, s11
	ds_write_b32 v2, v1
	s_or_b64 exec, exec, s[6:7]
	v_lshlrev_b32_e32 v150, 16, v88
	v_and_b32_e32 v151, 0xffff0000, v88
	v_lshlrev_b32_e32 v152, 16, v89
	v_and_b32_e32 v153, 0xffff0000, v89
	v_lshlrev_b32_e32 v146, 16, v86
	v_and_b32_e32 v147, 0xffff0000, v86
	v_lshlrev_b32_e32 v148, 16, v87
	v_and_b32_e32 v149, 0xffff0000, v87
	v_add_f32_e32 v1, v153, v152
	v_add_f32_e32 v86, v151, v150
	v_add_f32_e32 v1, v86, v1
	v_add_f32_e32 v86, v149, v148
	v_add_f32_e32 v87, v147, v146
	v_lshlrev_b32_e32 v142, 16, v92
	v_and_b32_e32 v143, 0xffff0000, v92
	v_lshlrev_b32_e32 v144, 16, v93
	v_and_b32_e32 v145, 0xffff0000, v93
	v_add_f32_e32 v86, v87, v86
	global_load_dwordx4 v[116:119], v[96:97], off offset:16
	global_load_dwordx4 v[120:123], v[96:97], off
	global_load_dwordx4 v[124:127], v[98:99], off offset:16
	global_load_dwordx4 v[128:131], v[98:99], off
	v_lshlrev_b32_e32 v2, 16, v90
	v_and_b32_e32 v3, 0xffff0000, v90
	v_lshlrev_b32_e32 v140, 16, v91
	v_and_b32_e32 v141, 0xffff0000, v91
	v_add_f32_e32 v1, v86, v1
	v_add_f32_e32 v86, v145, v144
	v_add_f32_e32 v87, v143, v142
	v_add_f32_e32 v86, v87, v86
	v_add_f32_e32 v87, v141, v140
	v_add_f32_e32 v88, v3, v2
	v_add_f32_e32 v87, v88, v87
	v_add_f32_e32 v86, v87, v86
	v_add_f32_e32 v1, v86, v1
	global_load_dwordx4 v[86:89], v[96:97], off offset:2064
	global_load_dwordx4 v[90:93], v[96:97], off offset:2048
	global_load_dwordx4 v[132:135], v[98:99], off offset:2064
	global_load_dwordx4 v[136:139], v[98:99], off offset:2048
	v_add_f32_dpp v1, v1, v1 quad_perm:[1,0,3,2] row_mask:0xf bank_mask:0xf bound_ctrl:1
	s_mov_b32 s6, 0xf800000
	s_nop 0
	v_add_f32_dpp v1, v1, v1 quad_perm:[2,3,0,1] row_mask:0xf bank_mask:0xf bound_ctrl:1
	s_nop 1
	v_add_f32_dpp v1, v1, v1 row_half_mirror row_mask:0xf bank_mask:0xf bound_ctrl:1
	s_nop 1
	v_add_f32_dpp v1, v1, v1 row_mirror row_mask:0xf bank_mask:0xf bound_ctrl:1
	ds_swizzle_b32 v154, v1 offset:swizzle(SWAP,16)
	s_waitcnt lgkmcnt(0)
; __device__ __forceinline__ float wave_sum(float v) { v += dpp_f<0xB1>(v); v += dpp_f<0x4E>(v); v += dpp_f<0x141>(v); v += dpp_f<0x140>(v); v += xor_sw<16>(v); return sum_x32(v); }
; __device__ __forceinline__ void ln_row16(float (&v)[16], const float* lng, const float* lnb, int lane, float (&o)[16]) {
;     const float s = ((v[0] + v[1]) + (v[2] + v[3])) + ((v[4] + v[5]) + (v[6] + v[7])) + (((v[8] + v[9]) + (v[10] + v[11])) + ((v[12] + v[13]) + (v[14] + v[15])));
;     const float mean = wave_sum(s) * (1.0f / D);
; #pragma unroll
;     for (int i = 0; i < 16; ++i) v[i] -= mean;
;     const float s2 = ((v[0] * v[0] + v[1] * v[1]) + (v[2] * v[2] + v[3] * v[3])) + ((v[4] * v[4] + v[5] * v[5]) + (v[6] * v[6] + v[7] * v[7]))
;                    + (((v[8] * v[8] + v[9] * v[9]) + (v[10] * v[10] + v[11] * v[11])) + ((v[12] * v[12] + v[13] * v[13]) + (v[14] * v[14] + v[15] * v[15])));
;     const float rstd = 1.0f / sqrtf(wave_sum(s2) * (1.0f / D) + LN_EPS);
; #pragma unroll
;     for (int hf = 0; hf < 2; ++hf) { const int col = 512 * hf + 8 * lane;
;         const f32x4 g0 = *(const f32x4*)(lng + col), g1 = *(const f32x4*)(lng + col + 4), b0 = *(const f32x4*)(lnb + col), b1 = *(const f32x4*)(lnb + col + 4);
; #pragma unroll
;         for (int i = 0; i < 4; ++i) { o[8 * hf + i] = v[8 * hf + i] * rstd * g0[i] + b0[i]; o[8 * hf + 4 + i] = v[8 * hf + 4 + i] * rstd * g1[i] + b1[i]; } }
; __global__ void __launch_bounds__(NWAVES * 64, 2) mk_fwd(Args args) {
;     ...
;                 {   const int bn = (bi + G < T / 16) ? bi + G : bi;
; #pragma unroll
;                     for (int ii = 0; ii < 2; ++ii) { const size_t t = (size_t)bn * 16 + wave * 2 + ii; yp[ii][0] = *(const u32x4*)(YB + t * D + 8 * lane); yp[ii][1] = *(const u32x4*)(YB + t * D + 512 + 8 * lane); } }
	v_add_f32_e32 v1, v1, v154
	v_mov_b32_e32 v154, v1
	s_nop 1
	v_permlane32_swap_b32_e32 v1, v154
	v_add_f32_e32 v1, v1, v154
	v_mul_f32_e32 v154, 0x3a800000, v1
	v_pk_add_f32 v[2:3], v[2:3], v[154:155] op_sel_hi:[1,0] neg_lo:[0,1] neg_hi:[0,1]
	v_pk_add_f32 v[140:141], v[140:141], v[154:155] op_sel_hi:[1,0] neg_lo:[0,1] neg_hi:[0,1]
	v_pk_add_f32 v[142:143], v[142:143], v[154:155] op_sel_hi:[1,0] neg_lo:[0,1] neg_hi:[0,1]
	v_pk_add_f32 v[144:145], v[144:145], v[154:155] op_sel_hi:[1,0] neg_lo:[0,1] neg_hi:[0,1]
	v_pk_add_f32 v[146:147], v[146:147], v[154:155] op_sel_hi:[1,0] neg_lo:[0,1] neg_hi:[0,1]
	v_pk_add_f32 v[148:149], v[148:149], v[154:155] op_sel_hi:[1,0] neg_lo:[0,1] neg_hi:[0,1]
	v_pk_add_f32 v[150:151], v[150:151], v[154:155] op_sel_hi:[1,0] neg_lo:[0,1] neg_hi:[0,1]
	v_pk_add_f32 v[152:153], v[152:153], v[154:155] op_sel_hi:[1,0] neg_lo:[0,1] neg_hi:[0,1]
	v_pk_mul_f32 v[154:155], v[2:3], v[2:3]
	v_pk_mul_f32 v[156:157], v[140:141], v[140:141]
	v_pk_mul_f32 v[158:159], v[142:143], v[142:143]
	v_pk_mul_f32 v[160:161], v[144:145], v[144:145]
	v_pk_mul_f32 v[162:163], v[146:147], v[146:147]
	v_pk_mul_f32 v[164:165], v[148:149], v[148:149]
	v_pk_mul_f32 v[166:167], v[150:151], v[150:151]
	v_pk_mul_f32 v[168:169], v[152:153], v[152:153]
	v_add_f32_e32 v166, v166, v167
	v_add_f32_e32 v1, v168, v169
	v_add_f32_e32 v164, v164, v165
	v_add_f32_e32 v162, v162, v163
	v_add_f32_e32 v160, v160, v161
	v_add_f32_e32 v158, v158, v159
	v_add_f32_e32 v156, v156, v157
	v_add_f32_e32 v154, v154, v155
	v_add_f32_e32 v1, v166, v1
	v_add_f32_e32 v162, v162, v164
	v_add_f32_e32 v158, v158, v160
	v_add_f32_e32 v154, v154, v156
	v_add_f32_e32 v1, v162, v1
	v_add_f32_e32 v154, v154, v158
	v_add_f32_e32 v1, v154, v1
	s_nop 1
	v_add_f32_dpp v1, v1, v1 quad_perm:[1,0,3,2] row_mask:0xf bank_mask:0xf bound_ctrl:1
	s_nop 1
	v_add_f32_dpp v1, v1, v1 quad_perm:[2,3,0,1] row_mask:0xf bank_mask:0xf bound_ctrl:1
	s_nop 1
	v_add_f32_dpp v1, v1, v1 row_half_mirror row_mask:0xf bank_mask:0xf bound_ctrl:1
	s_nop 1
	v_add_f32_dpp v1, v1, v1 row_mirror row_mask:0xf bank_mask:0xf bound_ctrl:1
	ds_swizzle_b32 v154, v1 offset:swizzle(SWAP,16)
	s_waitcnt lgkmcnt(0)
	v_add_f32_e32 v1, v1, v154
	v_mov_b32_e32 v154, v1
	s_nop 1
	v_permlane32_swap_b32_e32 v1, v154
	v_add_f32_e32 v1, v1, v154
	v_fmamk_f32 v1, v1, 0x3a800000, v250
	v_mul_f32_e32 v154, 0x4f800000, v1
	v_cmp_gt_f32_e32 vcc, s6, v1
	s_nop 1
	v_cndmask_b32_e32 v1, v1, v154, vcc
	v_sqrt_f32_e32 v154, v1
	s_nop 0
	v_add_u32_e32 v155, -1, v154
	v_fma_f32 v156, -v155, v154, v1
	v_cmp_ge_f32_e64 s[6:7], 0, v156
	v_add_u32_e32 v156, 1, v154
	s_nop 0
	v_cndmask_b32_e64 v155, v154, v155, s[6:7]
	v_fma_f32 v154, -v156, v154, v1
	v_cmp_lt_f32_e64 s[6:7], 0, v154
	s_nop 1
	v_cndmask_b32_e64 v154, v155, v156, s[6:7]
	v_mul_f32_e32 v155, 0x37800000, v154
	v_cndmask_b32_e32 v154, v154, v155, vcc
	v_cmp_class_f32_e32 vcc, v1, v251
	s_nop 1
	v_cndmask_b32_e32 v1, v154, v1, vcc
	v_div_scale_f32 v154, s[6:7], v1, v1, 1.0
	v_rcp_f32_e32 v155, v154
	v_readlane_b32 s6, v255, 21
	v_fma_f32 v156, -v154, v155, 1.0
	v_fmac_f32_e32 v155, v156, v155
	v_div_scale_f32 v156, vcc, 1.0, v1, 1.0
	v_mul_f32_e32 v157, v156, v155
	v_fma_f32 v158, -v154, v157, v156
	v_fmac_f32_e32 v157, v158, v155
	v_fma_f32 v154, -v154, v157, v156
	v_div_fmas_f32 v154, v154, v155, v157
	v_div_fixup_f32 v154, v154, v1, 1.0
	v_pk_mul_f32 v[2:3], v[2:3], v[154:155] op_sel_hi:[1,0]
	v_add_u32_e32 v1, s6, v113
	s_waitcnt vmcnt(4)
	v_pk_fma_f32 v[120:121], v[120:121], v[2:3], v[128:129]
	v_pk_mul_f32 v[2:3], v[142:143], v[154:155] op_sel_hi:[1,0]
	s_nop 0
	v_pk_fma_f32 v[116:117], v[116:117], v[2:3], v[124:125]
	v_pk_mul_f32 v[2:3], v[140:141], v[154:155] op_sel_hi:[1,0]
	s_nop 0
	v_pk_fma_f32 v[122:123], v[122:123], v[2:3], v[130:131]
	v_pk_mul_f32 v[2:3], v[144:145], v[154:155] op_sel_hi:[1,0]
	s_nop 0
	v_pk_fma_f32 v[118:119], v[118:119], v[2:3], v[126:127]
	v_pk_mul_f32 v[2:3], v[146:147], v[154:155] op_sel_hi:[1,0]
	s_waitcnt vmcnt(0)
	s_and_b64 vcc, exec, s[8:9]
	s_cbranch_vccnz .Lph3_no_prefetch
	v_lshl_add_u64 v[246:247], v[104:105], 0, s[98:99]
	global_load_dwordx4 v[74:77], v[246:247], off nt
	global_load_dwordx4 v[70:73], v[246:247], off offset:1024 nt
	global_load_dwordx4 v[78:81], v[246:247], off offset:2048 nt
	global_load_dwordx4 v[82:85], v[246:247], off offset:3072 nt
